# P2: half of the WGs run in-proj GEMM before expert-weight conversion (overlap HBM streaming with MFMA); real grid barrier before layer 1
# speedup vs baseline: 1.0219x; 1.0219x over previous
.LBB0_173:
	s_or_b64 exec, exec, s[2:3]
	s_mov_b64 s[8:9], 0x4c000
	s_mov_b64 s[6:7], 0x18acc000
	s_cmp_eq_u32 s36, 0
	s_cbranch_scc1 .Lseam1_l0
	s_mov_b64 s[6:7], 0x14a8c000
	s_mov_b64 s[8:9], 0x89cc000

.LBB0_174:
	s_lshl_b32 s22, s36, 20
	s_lshl_b32 s23, s36, 28
	s_waitcnt vmcnt(3)
	v_mov_b32_e32 v2, v0
	s_mov_b64 s[0:1], s[42:43]
	s_add_u32 s19, s0, 0x10a4c000
	s_addc_u32 s20, s1, 0
	s_add_u32 s2, s0, 0x14a4c000
	s_addc_u32 s3, s1, 0
	s_add_u32 s4, s0, 0x894c000
	s_addc_u32 s5, s1, 0
	v_readfirstlane_b32 s10, v2
	s_add_u32 s21, s0, 0x94c000
	s_addc_u32 s24, s1, 0
	v_lshlrev_b32_e32 v3, 1, v2
	s_ashr_i32 s0, s10, 1
	v_and_b32_e32 v70, 0x70, v3
	s_and_b32 s10, s0, 0xffffffe0
	v_lshlrev_b32_e32 v3, 2, v2
	v_lshlrev_b32_e32 v2, 6, v2
	s_lshr_b32 s0, s0, 1
	s_mov_b32 s18, s85
	s_mov_b32 s26, s95
	v_and_b32_e32 v72, 28, v3
	v_and_b32_e32 v2, 0x80, v2
	s_and_b32 s0, s0, 0x60
	v_and_b32_e32 v3, 4, v3
	s_mov_b32 s25, 20
	s_ashr_i32 s11, s10, 31
	v_or3_b32 v67, v3, v2, s0
	v_mov_b32_e32 v71, v69
	v_or_b32_e32 v73, s0, v2
	s_mov_b32 s27, s26
	s_bfe_u32 s100, s95, 0x10003
	s_mov_b32 s101, 0
	s_cmp_eq_u32 s100, 0
	s_cbranch_scc0 .LBB0_302
	s_branch .LBB0_177

.LBB0_302:
	s_cmp_eq_u32 s101, 1
	s_cbranch_scc1 .LBB0_431
	v_mov_b32_e32 v4, v0
	s_barrier
	s_mov_b64 s[0:1], s[42:43]
	s_mov_b32 s11, s95
	s_mov_b32 s10, s85
	v_cmp_gt_i32_e32 vcc, 24, v4
	s_barrier
	s_and_saveexec_b64 s[0:1], vcc
	s_cbranch_execz .LBB0_310
	s_ashr_i32 s2, s11, 31
	v_mov_b32_e32 v2, s11
	v_mov_b32_e32 v3, s2
	v_mad_i64_i32 v[2:3], s[2:3], s10, v4, v[2:3]
	s_mov_b64 s[2:3], 0x6b4
	s_nop 0
	v_cmp_gt_i64_e32 vcc, s[2:3], v[2:3]
	s_and_saveexec_b64 s[4:5], vcc
	s_cbranch_execz .LBB0_309
	v_ashrrev_i32_e32 v3, 31, v2
	v_lshrrev_b32_e32 v3, 29, v3
	v_add_u32_e32 v5, v2, v3
	v_and_b32_e32 v3, -8, v5
	v_sub_u32_e32 v3, v2, v3
	v_cmp_lt_i32_e64 s[2:3], 3, v3
	s_and_saveexec_b64 s[12:13], s[2:3]
	s_xor_b64 s[2:3], exec, s[12:13]
	s_movk_i32 s12, 0xd6
	v_mad_u64_u32 v[2:3], s[12:13], v3, s12, 4
	s_andn2_saveexec_b64 s[2:3], s[2:3]
	s_movk_i32 s12, 0xd7
	v_mul_lo_u32 v2, v3, s12
	s_or_b64 exec, exec, s[2:3]
	v_ashrrev_i32_e32 v3, 3, v5
	v_add_u32_e32 v2, v2, v3
	s_mov_b32 s2, 0x4ec4ec4f
	v_mul_hi_i32 v3, v2, s2
	v_lshrrev_b32_e32 v5, 31, v3
	v_ashrrev_i32_e32 v3, 5, v3
	v_add_u32_e32 v3, v3, v5
	v_lshlrev_b32_e32 v5, 3, v3
	s_waitcnt vmcnt(2)
	v_sub_u32_e32 v6, 0x84, v5
	v_min_i32_e32 v6, 8, v6
	v_sub_u32_e32 v7, 0, v6
	v_max_i32_e32 v7, v6, v7
	v_cvt_f32_u32_e32 v8, v7
	s_movk_i32 s2, 0x68
	v_mul_lo_u32 v3, v3, s2
	s_waitcnt vmcnt(1)
	v_sub_u32_e32 v10, 0, v7
	v_rcp_iflag_f32_e32 v8, v8
	v_sub_u32_e32 v2, v2, v3
	v_sub_u32_e32 v3, 0, v2
	v_max_i32_e32 v3, v2, v3
	v_mul_f32_e32 v8, 0x4f7ffffe, v8
	v_cvt_u32_f32_e32 v8, v8
	v_xor_b32_e32 v9, v2, v6
	v_ashrrev_i32_e32 v9, 31, v9
	v_mul_lo_u32 v10, v10, v8
	v_mul_hi_u32 v10, v8, v10
	v_add_u32_e32 v8, v8, v10
	v_mul_hi_u32 v8, v3, v8
	v_mul_lo_u32 v10, v8, v7
	v_sub_u32_e32 v3, v3, v10
	v_add_u32_e32 v11, 1, v8
	v_cmp_ge_u32_e64 s[2:3], v3, v7
	v_sub_u32_e32 v10, v3, v7
	s_nop 0
	v_cndmask_b32_e64 v8, v8, v11, s[2:3]
	v_cndmask_b32_e64 v3, v3, v10, s[2:3]
	v_add_u32_e32 v10, 1, v8
	v_cmp_ge_u32_e64 s[2:3], v3, v7
	s_nop 1
	v_cndmask_b32_e64 v3, v8, v10, s[2:3]
	v_xor_b32_e32 v3, v3, v9
	v_sub_u32_e32 v3, v3, v9
	v_mul_lo_u32 v6, v3, v6
	v_sub_u32_e32 v2, v2, v6
	v_add_u32_e32 v5, v5, v2

.LBB0_430:
	s_movk_i32 s34, 0x1000
	s_barrier
	s_cmp_eq_u32 s100, 1
	s_cbranch_scc0 .LBB0_431
	s_mov_b32 s101, 1
	s_lshl_b32 s22, s36, 20
	s_lshl_b32 s23, s36, 28
	s_waitcnt vmcnt(3)
	v_mov_b32_e32 v2, v0
	s_mov_b64 s[0:1], s[42:43]
	s_add_u32 s19, s0, 0x10a4c000
	s_addc_u32 s20, s1, 0
	s_add_u32 s2, s0, 0x14a4c000
	s_addc_u32 s3, s1, 0
	s_add_u32 s4, s0, 0x894c000
	s_addc_u32 s5, s1, 0
	v_readfirstlane_b32 s10, v2
	s_add_u32 s21, s0, 0x94c000
	s_addc_u32 s24, s1, 0
	v_lshlrev_b32_e32 v3, 1, v2
	s_ashr_i32 s0, s10, 1
	v_and_b32_e32 v70, 0x70, v3
	s_and_b32 s10, s0, 0xffffffe0
	v_lshlrev_b32_e32 v3, 2, v2
	v_lshlrev_b32_e32 v2, 6, v2
	s_lshr_b32 s0, s0, 1
	s_mov_b32 s18, s85
	s_mov_b32 s26, s95
	v_and_b32_e32 v72, 28, v3
	v_and_b32_e32 v2, 0x80, v2
	s_and_b32 s0, s0, 0x60
	v_and_b32_e32 v3, 4, v3
	s_mov_b32 s25, 20
	s_ashr_i32 s11, s10, 31
	v_or3_b32 v67, v3, v2, s0
	v_mov_b32_e32 v71, v69
	v_or_b32_e32 v73, s0, v2
	s_mov_b32 s27, s26
	s_branch .LBB0_177

	.amdhsa_kernel _Z6mk_fwd4Args
		.amdhsa_group_segment_fixed_size 0
		.amdhsa_private_segment_fixed_size 0
		.amdhsa_kernarg_size 472
		.amdhsa_user_sgpr_count 2
		.amdhsa_user_sgpr_dispatch_ptr 0
		.amdhsa_user_sgpr_queue_ptr 0
		.amdhsa_user_sgpr_kernarg_segment_ptr 1
		.amdhsa_user_sgpr_dispatch_id 0
		.amdhsa_user_sgpr_kernarg_preload_length 0
		.amdhsa_user_sgpr_kernarg_preload_offset 0
		.amdhsa_user_sgpr_private_segment_size 0
		.amdhsa_uses_dynamic_stack 0
		.amdhsa_enable_private_segment 0
		.amdhsa_system_sgpr_workgroup_id_x 1
		.amdhsa_system_sgpr_workgroup_id_y 0
		.amdhsa_system_sgpr_workgroup_id_z 0
		.amdhsa_system_sgpr_workgroup_info 0
		.amdhsa_system_vgpr_workitem_id 0
		.amdhsa_next_free_vgpr 248
		.amdhsa_next_free_sgpr 102
		.amdhsa_accum_offset 248
		.amdhsa_reserve_vcc 1
		.amdhsa_float_round_mode_32 0
		.amdhsa_float_round_mode_16_64 0
		.amdhsa_float_denorm_mode_32 3
		.amdhsa_float_denorm_mode_16_64 3
		.amdhsa_dx10_clamp 1
		.amdhsa_ieee_mode 1
		.amdhsa_fp16_overflow 0
		.amdhsa_tg_split 0
		.amdhsa_exception_fp_ieee_invalid_op 0
		.amdhsa_exception_fp_denorm_src 0
		.amdhsa_exception_fp_ieee_div_zero 0
		.amdhsa_exception_fp_ieee_overflow 0
		.amdhsa_exception_fp_ieee_underflow 0
		.amdhsa_exception_fp_ieee_inexact 0
		.amdhsa_exception_int_div_zero 0
	.end_amdhsa_kernel

amdhsa.kernels:
  - .agpr_count:     0
    .args:
      - .offset:         0
        .size:           216
        .value_kind:     by_value
      - .offset:         216
        .size:           4
        .value_kind:     hidden_block_count_x
      - .offset:         220
        .size:           4
        .value_kind:     hidden_block_count_y
      - .offset:         224
        .size:           4
        .value_kind:     hidden_block_count_z
      - .offset:         228
        .size:           2
        .value_kind:     hidden_group_size_x
      - .offset:         230
        .size:           2
        .value_kind:     hidden_group_size_y
      - .offset:         232
        .size:           2
        .value_kind:     hidden_group_size_z
      - .offset:         234
        .size:           2
        .value_kind:     hidden_remainder_x
      - .offset:         236
        .size:           2
        .value_kind:     hidden_remainder_y
      - .offset:         238
        .size:           2
        .value_kind:     hidden_remainder_z
      - .offset:         256
        .size:           8
        .value_kind:     hidden_global_offset_x
      - .offset:         264
        .size:           8
        .value_kind:     hidden_global_offset_y
      - .offset:         272
        .size:           8
        .value_kind:     hidden_global_offset_z
      - .offset:         280
        .size:           2
        .value_kind:     hidden_grid_dims
      - .offset:         336
        .size:           4
        .value_kind:     hidden_dynamic_lds_size
    .group_segment_fixed_size: 0
    .kernarg_segment_align: 8
    .kernarg_segment_size: 472
    .language:       OpenCL C
    .language_version:
      - 2
      - 0
    .max_flat_workgroup_size: 512
    .name:           _Z6mk_fwd4Args
    .private_segment_fixed_size: 0
    .sgpr_count:     108
    .sgpr_spill_count: 43
    .symbol:         _Z6mk_fwd4Args.kd
    .uniform_work_group_size: 1
    .uses_dynamic_stack: false
    .vgpr_count:     248
    .vgpr_spill_count: 0
    .wavefront_size: 64
